# expert row-tile prefix table: the 32 expert counters loaded together instead of 32 dependent round trips
# speedup vs baseline: 1.0133x; 1.0010x over previous
; __device__ __forceinline__ void build_tstart(Frame& F, LAS int* tstart) {
;     if (FTID == 0) { int s = 0; for (int e = 0; e < NE; ++e) { tstart[e] = s; const unsigned n = __hip_atomic_load(F.ctl + CW_CNT + 64 * e, RLX_AGENT); s += (int)((n + 255u) >> 8); } tstart[NE] = s; }
.LBB0_1563:
	s_and_b64 vcc, exec, s[4:5]
	s_cbranch_vccz .LBB0_1570
	s_waitcnt vmcnt(0)
	v_mbcnt_lo_u32_b32 v0, -1, 0
	v_mbcnt_hi_u32_b32 v0, -1, v0
	s_nop 0
	v_sub_u32_e32 v0, 0, v0
	v_cmp_eq_u32_e32 vcc, s88, v0
	s_and_saveexec_b64 s[4:5], vcc
	s_cbranch_execz .LBB0_1566
	v_mov_b32_e32 v228, 0x24040
	v_mov_b32_e32 v0, 0
	ds_write_b32 v228, v0
	v_mov_b32_e32 v229, 0x8000
	v_mov_b32_e32 v230, 0x9000
	global_load_dword v196, v229, s[28:29] sc1
	global_load_dword v197, v229, s[28:29] offset:256 sc1
	global_load_dword v198, v229, s[28:29] offset:512 sc1
	global_load_dword v199, v229, s[28:29] offset:768 sc1
	global_load_dword v200, v229, s[28:29] offset:1024 sc1
	global_load_dword v201, v229, s[28:29] offset:1280 sc1
	global_load_dword v202, v229, s[28:29] offset:1536 sc1
	global_load_dword v203, v229, s[28:29] offset:1792 sc1
	global_load_dword v204, v229, s[28:29] offset:2048 sc1
	global_load_dword v205, v229, s[28:29] offset:2304 sc1
	global_load_dword v206, v229, s[28:29] offset:2560 sc1
	global_load_dword v207, v229, s[28:29] offset:2816 sc1
	global_load_dword v208, v229, s[28:29] offset:3072 sc1
	global_load_dword v209, v229, s[28:29] offset:3328 sc1
	global_load_dword v210, v229, s[28:29] offset:3584 sc1
	global_load_dword v211, v229, s[28:29] offset:3840 sc1
	global_load_dword v212, v230, s[28:29] sc1
	global_load_dword v213, v230, s[28:29] offset:256 sc1
	global_load_dword v214, v230, s[28:29] offset:512 sc1
	global_load_dword v215, v230, s[28:29] offset:768 sc1
	global_load_dword v216, v230, s[28:29] offset:1024 sc1
	global_load_dword v217, v230, s[28:29] offset:1280 sc1
	global_load_dword v218, v230, s[28:29] offset:1536 sc1
	global_load_dword v219, v230, s[28:29] offset:1792 sc1
	global_load_dword v220, v230, s[28:29] offset:2048 sc1
	global_load_dword v221, v230, s[28:29] offset:2304 sc1
	global_load_dword v222, v230, s[28:29] offset:2560 sc1
	global_load_dword v223, v230, s[28:29] offset:2816 sc1
	global_load_dword v224, v230, s[28:29] offset:3072 sc1
	global_load_dword v225, v230, s[28:29] offset:3328 sc1
	global_load_dword v226, v230, s[28:29] offset:3584 sc1
	global_load_dword v227, v230, s[28:29] offset:3840 sc1
	s_waitcnt vmcnt(0)
	v_add_u32_e32 v196, 0xff, v196
	v_lshrrev_b32_e32 v196, 8, v196
	v_add_u32_e32 v0, v196, v0
	ds_write_b32 v228, v0 offset:4
	v_add_u32_e32 v197, 0xff, v197
	v_lshrrev_b32_e32 v197, 8, v197
	v_add_u32_e32 v0, v197, v0
	ds_write_b32 v228, v0 offset:8
	v_add_u32_e32 v198, 0xff, v198
	v_lshrrev_b32_e32 v198, 8, v198
	v_add_u32_e32 v0, v198, v0
	ds_write_b32 v228, v0 offset:12
	v_add_u32_e32 v199, 0xff, v199
	v_lshrrev_b32_e32 v199, 8, v199
	v_add_u32_e32 v0, v199, v0
	ds_write_b32 v228, v0 offset:16
	v_add_u32_e32 v200, 0xff, v200
	v_lshrrev_b32_e32 v200, 8, v200
	v_add_u32_e32 v0, v200, v0
	ds_write_b32 v228, v0 offset:20
	v_add_u32_e32 v201, 0xff, v201
	v_lshrrev_b32_e32 v201, 8, v201
	v_add_u32_e32 v0, v201, v0
	ds_write_b32 v228, v0 offset:24
	v_add_u32_e32 v202, 0xff, v202
	v_lshrrev_b32_e32 v202, 8, v202
	v_add_u32_e32 v0, v202, v0
	ds_write_b32 v228, v0 offset:28
	v_add_u32_e32 v203, 0xff, v203
	v_lshrrev_b32_e32 v203, 8, v203
	v_add_u32_e32 v0, v203, v0
	ds_write_b32 v228, v0 offset:32
	v_add_u32_e32 v204, 0xff, v204
	v_lshrrev_b32_e32 v204, 8, v204
	v_add_u32_e32 v0, v204, v0
	ds_write_b32 v228, v0 offset:36
	v_add_u32_e32 v205, 0xff, v205
	v_lshrrev_b32_e32 v205, 8, v205
	v_add_u32_e32 v0, v205, v0
	ds_write_b32 v228, v0 offset:40
	v_add_u32_e32 v206, 0xff, v206
	v_lshrrev_b32_e32 v206, 8, v206
	v_add_u32_e32 v0, v206, v0
	ds_write_b32 v228, v0 offset:44
	v_add_u32_e32 v207, 0xff, v207
	v_lshrrev_b32_e32 v207, 8, v207
	v_add_u32_e32 v0, v207, v0
	ds_write_b32 v228, v0 offset:48
	v_add_u32_e32 v208, 0xff, v208
	v_lshrrev_b32_e32 v208, 8, v208
	v_add_u32_e32 v0, v208, v0
	ds_write_b32 v228, v0 offset:52
	v_add_u32_e32 v209, 0xff, v209
	v_lshrrev_b32_e32 v209, 8, v209
	v_add_u32_e32 v0, v209, v0
	ds_write_b32 v228, v0 offset:56
	v_add_u32_e32 v210, 0xff, v210
	v_lshrrev_b32_e32 v210, 8, v210
	v_add_u32_e32 v0, v210, v0
	ds_write_b32 v228, v0 offset:60
	v_add_u32_e32 v211, 0xff, v211
	v_lshrrev_b32_e32 v211, 8, v211
	v_add_u32_e32 v0, v211, v0
	ds_write_b32 v228, v0 offset:64
	v_add_u32_e32 v212, 0xff, v212
	v_lshrrev_b32_e32 v212, 8, v212
	v_add_u32_e32 v0, v212, v0
	ds_write_b32 v228, v0 offset:68
	v_add_u32_e32 v213, 0xff, v213
	v_lshrrev_b32_e32 v213, 8, v213
	v_add_u32_e32 v0, v213, v0
	ds_write_b32 v228, v0 offset:72
	v_add_u32_e32 v214, 0xff, v214
	v_lshrrev_b32_e32 v214, 8, v214
	v_add_u32_e32 v0, v214, v0
	ds_write_b32 v228, v0 offset:76
	v_add_u32_e32 v215, 0xff, v215
	v_lshrrev_b32_e32 v215, 8, v215
	v_add_u32_e32 v0, v215, v0
	ds_write_b32 v228, v0 offset:80
	v_add_u32_e32 v216, 0xff, v216
	v_lshrrev_b32_e32 v216, 8, v216
	v_add_u32_e32 v0, v216, v0
	ds_write_b32 v228, v0 offset:84
	v_add_u32_e32 v217, 0xff, v217
	v_lshrrev_b32_e32 v217, 8, v217
	v_add_u32_e32 v0, v217, v0
	ds_write_b32 v228, v0 offset:88
	v_add_u32_e32 v218, 0xff, v218
	v_lshrrev_b32_e32 v218, 8, v218
	v_add_u32_e32 v0, v218, v0
	ds_write_b32 v228, v0 offset:92
	v_add_u32_e32 v219, 0xff, v219
	v_lshrrev_b32_e32 v219, 8, v219
	v_add_u32_e32 v0, v219, v0
	ds_write_b32 v228, v0 offset:96
	v_add_u32_e32 v220, 0xff, v220
	v_lshrrev_b32_e32 v220, 8, v220
	v_add_u32_e32 v0, v220, v0
	ds_write_b32 v228, v0 offset:100
	v_add_u32_e32 v221, 0xff, v221
	v_lshrrev_b32_e32 v221, 8, v221
	v_add_u32_e32 v0, v221, v0
	ds_write_b32 v228, v0 offset:104
	v_add_u32_e32 v222, 0xff, v222
	v_lshrrev_b32_e32 v222, 8, v222
	v_add_u32_e32 v0, v222, v0
	ds_write_b32 v228, v0 offset:108
	v_add_u32_e32 v223, 0xff, v223
	v_lshrrev_b32_e32 v223, 8, v223
	v_add_u32_e32 v0, v223, v0
	ds_write_b32 v228, v0 offset:112
	v_add_u32_e32 v224, 0xff, v224
	v_lshrrev_b32_e32 v224, 8, v224
	v_add_u32_e32 v0, v224, v0
	ds_write_b32 v228, v0 offset:116
	v_add_u32_e32 v225, 0xff, v225
	v_lshrrev_b32_e32 v225, 8, v225
	v_add_u32_e32 v0, v225, v0
	ds_write_b32 v228, v0 offset:120
	v_add_u32_e32 v226, 0xff, v226
	v_lshrrev_b32_e32 v226, 8, v226
	v_add_u32_e32 v0, v226, v0
	ds_write_b32 v228, v0 offset:124
	v_add_u32_e32 v227, 0xff, v227
	v_lshrrev_b32_e32 v227, 8, v227
	v_add_u32_e32 v0, v227, v0
	ds_write_b32 v228, v0 offset:128
	s_add_i32 s0, 0, 0x240c0
